# baseline (speedup 1.0000x reference)
.LBB1_15:
	v_readfirstlane_b32 s86, v172
	v_readfirstlane_b32 s87, v173
	v_readfirstlane_b32 s88, v174
	v_readfirstlane_b32 s89, v175
	v_lshrrev_b32_e32 v232, 3, v198
	v_and_b32_e32 v233, 7, v198
	v_xor_b32_e32 v233, v233, v232
	s_and_b32 s84, s27, 0x7ff
	s_lshr_b32 s85, s62, 1
	s_lshl_b32 s85, s85, 7
	s_add_i32 s84, s84, s85
	s_and_b32 s85, s62, 1
	s_lshl_b32 s85, s85, 5
	s_add_i32 s84, s84, s85
	v_add_u32_e32 v232, s84, v232
	v_lshlrev_b32_e32 v232, 7, v232
	v_lshl_add_u32 v232, v233, 4, v232
	s_bfe_u32 s91, s27, 0x10006
	s_lshl_b32 s90, s91, 2
	s_add_i32 s90, s90, s62
	s_lshl_b32 s90, s90, 10
	s_add_u32 s92, s86, 0x0
	s_addc_u32 s93, s87, 0
	s_add_i32 m0, s90, 0x0
	s_nop 0
	global_load_lds_dwordx4 v232, s[92:93]
	s_add_u32 s92, s86, 0x400
	s_addc_u32 s93, s87, 0
	s_add_i32 m0, s90, 0x2000
	s_nop 0
	global_load_lds_dwordx4 v232, s[92:93]
	s_add_u32 s92, s86, 0x800
	s_addc_u32 s93, s87, 0
	s_add_i32 m0, s90, 0x4000
	s_nop 0
	global_load_lds_dwordx4 v232, s[92:93]
	s_add_u32 s92, s86, 0xc00
	s_addc_u32 s93, s87, 0
	s_add_i32 m0, s90, 0x6000
	s_nop 0
	global_load_lds_dwordx4 v232, s[92:93]
	s_add_u32 s92, s88, 0x0
	s_addc_u32 s93, s89, 0
	s_add_i32 m0, s90, 0x8000
	s_nop 0
	global_load_lds_dwordx4 v232, s[92:93]
	s_add_u32 s92, s88, 0x400
	s_addc_u32 s93, s89, 0
	s_add_i32 m0, s90, 0xa000
	s_nop 0
	global_load_lds_dwordx4 v232, s[92:93]
	s_add_u32 s92, s88, 0x800
	s_addc_u32 s93, s89, 0
	s_add_i32 m0, s90, 0xc000
	s_nop 0
	global_load_lds_dwordx4 v232, s[92:93]
	s_add_u32 s92, s88, 0xc00
	s_addc_u32 s93, s89, 0
	s_add_i32 m0, s90, 0xe000
	s_nop 0
	global_load_lds_dwordx4 v232, s[92:93]
	v_and_b32_e32 v234, 15, v198
	v_lshrrev_b32_e32 v235, 4, v198
	v_and_b32_e32 v236, 7, v234
	v_lshrrev_b32_e32 v237, 3, v234
	v_lshlrev_b32_e32 v238, 1, v235
	v_xor_b32_e32 v239, v238, v236
	v_or_b32_e32 v238, 1, v238
	v_xor_b32_e32 v238, v238, v236
	v_lshlrev_b32_e32 v237, 13, v237
	v_lshl_add_u32 v237, v236, 7, v237
	s_lshl_b32 s91, s91, 12
	v_add_u32_e32 v237, s91, v237
	v_lshl_add_u32 v244, v239, 4, v237
	v_lshl_add_u32 v245, v238, 4, v237
	s_waitcnt vmcnt(0)
	s_barrier
	s_cmp_gt_i32 s77, 7
	s_cselect_b64 s[52:53], -1, 0
	s_lshl_b32 s4, s77, 2
	s_add_i32 s78, s4, s66
	s_or_b32 s37, s4, s62
	s_lshr_b32 s4, s27, 8
	s_and_b32 s4, s4, 0x7ff8
	v_and_b32_e32 v147, 64, v198
	s_add_i32 s10, s4, s78
	s_lshr_b32 s4, s27, 6
	v_xor_b32_e32 v146, 16, v198
	v_add_u32_e32 v206, 64, v147
	s_and_b32 s4, s4, 0x7fe0
	v_cmp_lt_i32_e32 vcc, v146, v206
	s_add_i32 s54, s4, s37
	s_cmp_lt_i32 s77, 8
	v_cndmask_b32_e32 v146, v198, v146, vcc
	v_lshlrev_b32_e32 v201, 2, v146
	v_mul_f32_e32 v146, v127, v127
	v_mul_f32_e32 v147, v129, v129
	s_cselect_b64 s[6:7], -1, 0
	v_fmac_f32_e32 v146, v126, v126
	v_fmac_f32_e32 v147, v128, v128
	s_and_b64 s[4:5], s[6:7], exec
	v_add_f32_e32 v153, v146, v147
	v_pk_mul_f32 v[146:147], v[124:125], v[124:125]
	v_pk_mul_f32 v[148:149], v[122:123], v[122:123]
	s_cselect_b32 s9, s23, s25
	s_cselect_b32 s8, s22, s24
	v_and_b32_e32 v152, 0x7cf, v199
	v_mov_b32_e32 v150, v146
	v_mov_b32_e32 v151, v148
	v_mov_b32_e32 v148, v147
	global_load_dwordx4 v[138:141], v194, s[8:9] offset:16
	global_load_dwordx4 v[142:145], v194, s[8:9]
	global_load_dwordx4 v[130:133], v194, s[8:9] offset:144
	global_load_dwordx4 v[134:137], v194, s[8:9] offset:128
	v_pk_add_f32 v[146:147], v[150:151], v[148:149]
	v_lshlrev_b32_e32 v170, 7, v152
	v_add_f32_e32 v147, v153, v147
	v_add_f32_e32 v207, v146, v147
	ds_read_b128 v[146:149], v245 offset:32768
	s_nop 0
	ds_read_b128 v[150:153], v244 offset:32768
	s_nop 0
	ds_read_b128 v[154:157], v245 offset:0
	s_nop 0
	ds_read_b128 v[158:161], v244 offset:0
	v_pk_mul_f32 v[184:185], v[112:113], v[112:113]
	v_pk_mul_f32 v[202:203], v[110:111], v[110:111]
	v_mov_b32_e32 v204, v184
	v_mov_b32_e32 v205, v202
	v_mov_b32_e32 v202, v185
	v_pk_add_f32 v[184:185], v[204:205], v[202:203]
	v_pk_mul_f32 v[202:203], v[106:107], v[106:107]
	v_add_f32_e32 v170, v207, v185
	v_add_f32_e32 v170, v184, v170
	v_pk_mul_f32 v[184:185], v[108:109], v[108:109]
	v_mov_b32_e32 v205, v202
	v_mov_b32_e32 v204, v184
	v_mov_b32_e32 v202, v185
	v_pk_add_f32 v[184:185], v[204:205], v[202:203]
	v_cndmask_b32_e64 v200, 1.0, v197, s[6:7]
	v_add_f32_e32 v170, v185, v170
	v_add_f32_e32 v170, v184, v170
	ds_bpermute_b32 v184, v201, v170
	v_xor_b32_e32 v185, 32, v198
	v_cmp_lt_i32_e32 vcc, v185, v206
	s_cselect_b32 s55, s17, s19
	v_or_b32_e32 v229, 16, v199
	v_cndmask_b32_e32 v185, v198, v185, vcc
	v_lshlrev_b32_e32 v202, 2, v185
	s_waitcnt lgkmcnt(0)
	v_add_f32_e32 v170, v170, v184
	ds_bpermute_b32 v184, v202, v170
	s_waitcnt lgkmcnt(0)
	v_add_f32_e32 v170, v170, v184
	v_fmamk_f32 v170, v170, 0x3c800000, v195
	v_rsq_f32_e32 v240, v170
	s_nop 0
	v_mul_f32_e32 v242, v170, v240
	v_fma_f32 v242, -v242, v240, 1.0
	v_mul_f32_e32 v243, 0.5, v240
	v_fmac_f32_e32 v240, v242, v243
	v_mul_f32_e32 v170, v200, v240
	v_lshl_or_b32 v203, s10, 17, v187
	v_lshl_or_b32 v185, s54, 17, v188
	s_cselect_b32 s54, s16, s18
	s_cselect_b32 s10, s72, 0x1000
	v_pk_mul_f32 v[216:217], v[106:107], v[170:171] op_sel_hi:[1,0]
	v_pk_mul_f32 v[210:211], v[122:123], v[170:171] op_sel_hi:[1,0]
	s_waitcnt vmcnt(0)
	v_pk_mul_f32 v[216:217], v[130:131], v[216:217]
	v_pk_mul_f32 v[210:211], v[138:139], v[210:211]
	v_pk_mul_f32 v[224:225], v[146:147], v[216:217]
	v_pk_mul_f32 v[212:213], v[110:111], v[170:171] op_sel_hi:[1,0]
	v_pk_fma_f32 v[224:225], v[154:155], v[210:211], v[224:225] neg_lo:[0,0,1] neg_hi:[0,0,1]
	v_pk_mul_f32 v[154:155], v[154:155], v[216:217]
	v_pk_mul_f32 v[214:215], v[112:113], v[170:171] op_sel_hi:[1,0]
	v_pk_mul_f32 v[218:219], v[108:109], v[170:171] op_sel_hi:[1,0]
	v_pk_fma_f32 v[154:155], v[146:147], v[210:211], v[154:155]
	v_lshlrev_b32_e32 v146, 6, v199
	v_pk_mul_f32 v[204:205], v[128:129], v[170:171] op_sel_hi:[1,0]
	v_pk_mul_f32 v[206:207], v[126:127], v[170:171] op_sel_hi:[1,0]
	v_pk_mul_f32 v[208:209], v[124:125], v[170:171] op_sel_hi:[1,0]
	v_pk_mul_f32 v[214:215], v[136:137], v[214:215]
	v_pk_mul_f32 v[212:213], v[134:135], v[212:213]
	v_pk_mul_f32 v[218:219], v[132:133], v[218:219]
	v_cndmask_b32_e64 v184, v203, v185, s[6:7]
	v_and_b32_e32 v228, 0x1f000, v146
	v_pk_mul_f32 v[206:207], v[142:143], v[206:207]
	v_pk_mul_f32 v[204:205], v[144:145], v[204:205]
	v_pk_mul_f32 v[208:209], v[140:141], v[208:209]
	v_pk_mul_f32 v[220:221], v[150:151], v[212:213]
	v_pk_mul_f32 v[222:223], v[152:153], v[214:215]
	v_pk_mul_f32 v[226:227], v[148:149], v[218:219]
	v_or3_b32 v146, v228, v189, v184
	v_pk_fma_f32 v[222:223], v[160:161], v[204:205], v[222:223] neg_lo:[0,0,1] neg_hi:[0,0,1]
	v_pk_fma_f32 v[220:221], v[158:159], v[206:207], v[220:221] neg_lo:[0,0,1] neg_hi:[0,0,1]
	v_pk_fma_f32 v[226:227], v[156:157], v[208:209], v[226:227] neg_lo:[0,0,1] neg_hi:[0,0,1]
	v_pk_mul_f32 v[158:159], v[158:159], v[212:213]
	v_pk_mul_f32 v[160:161], v[160:161], v[214:215]
	v_pk_mul_f32 v[156:157], v[156:157], v[218:219]
	v_ashrrev_i32_e32 v147, 31, v146
	v_pk_fma_f32 v[152:153], v[152:153], v[204:205], v[160:161]
	v_pk_fma_f32 v[150:151], v[150:151], v[206:207], v[158:159]
	v_pk_fma_f32 v[156:157], v[148:149], v[208:209], v[156:157]
	v_lshl_add_u64 v[158:159], v[146:147], 1, s[54:55]
	v_cvt_pk_f16_f32 v146, v220, v221
	v_cvt_pk_f16_f32 v147, v222, v223
	v_cvt_pk_f16_f32 v148, v224, v225
	v_cvt_pk_f16_f32 v149, v226, v227
	v_cvt_pk_f16_f32 v150, v150, v151
	v_cvt_pk_f16_f32 v151, v152, v153
	v_cvt_pk_f16_f32 v152, v154, v155
	v_cvt_pk_f16_f32 v153, v156, v157
	global_store_dwordx4 v[158:159], v[146:149], off sc1
	v_pk_mul_f32 v[204:205], v[96:97], v[96:97]
	v_pk_mul_f32 v[206:207], v[94:95], v[94:95]
	v_lshl_add_u64 v[146:147], v[158:159], 0, s[10:11]
	global_store_dwordx4 v[146:147], v[150:153], off sc1
	v_mul_f32_e32 v146, v119, v119
	v_mul_f32_e32 v147, v121, v121
	v_fmac_f32_e32 v146, v118, v118
	v_fmac_f32_e32 v147, v120, v120
	v_add_f32_e32 v153, v146, v147
	v_pk_mul_f32 v[146:147], v[116:117], v[116:117]
	v_pk_mul_f32 v[148:149], v[114:115], v[114:115]
	v_bitop3_b32 v152, v199, s73, 16 bitop3:0xc8
	v_mov_b32_e32 v150, v146
	v_mov_b32_e32 v151, v148
	v_mov_b32_e32 v148, v147
	v_pk_add_f32 v[146:147], v[150:151], v[148:149]
	v_lshlrev_b32_e32 v170, 7, v152
	v_add_f32_e32 v147, v153, v147
	v_add_f32_e32 v210, v146, v147
	ds_read_b128 v[146:149], v245 offset:49152
	s_nop 0
	ds_read_b128 v[150:153], v244 offset:49152
	s_nop 0
	ds_read_b128 v[154:157], v245 offset:16384
	s_nop 0
	ds_read_b128 v[158:161], v244 offset:16384
	v_mov_b32_e32 v208, v204
	v_mov_b32_e32 v209, v206
	v_mov_b32_e32 v206, v205
	v_pk_add_f32 v[204:205], v[208:209], v[206:207]
	v_pk_mul_f32 v[206:207], v[90:91], v[90:91]
	v_add_f32_e32 v170, v210, v205
	v_add_f32_e32 v170, v204, v170
	v_pk_mul_f32 v[204:205], v[92:93], v[92:93]
	v_mov_b32_e32 v209, v206
	v_mov_b32_e32 v208, v204
	v_mov_b32_e32 v206, v205
	v_pk_add_f32 v[204:205], v[208:209], v[206:207]
	s_nop 0
	v_add_f32_e32 v170, v205, v170
	v_add_f32_e32 v170, v204, v170
	ds_bpermute_b32 v204, v201, v170
	s_waitcnt lgkmcnt(0)
	v_add_f32_e32 v170, v170, v204
	ds_bpermute_b32 v204, v202, v170
	s_waitcnt lgkmcnt(0)
	v_add_f32_e32 v170, v170, v204
	v_fmamk_f32 v170, v170, 0x3c800000, v195
	v_rsq_f32_e32 v240, v170
	s_nop 0
	v_mul_f32_e32 v242, v170, v240
	v_fma_f32 v242, -v242, v240, 1.0
	v_mul_f32_e32 v243, 0.5, v240
	v_fmac_f32_e32 v240, v242, v243
	v_mul_f32_e32 v170, v200, v240
	s_mov_b64 s[8:9], -1
	v_pk_mul_f32 v[216:217], v[90:91], v[170:171] op_sel_hi:[1,0]
	v_pk_mul_f32 v[210:211], v[114:115], v[170:171] op_sel_hi:[1,0]
	v_pk_mul_f32 v[216:217], v[130:131], v[216:217]
	v_pk_mul_f32 v[210:211], v[138:139], v[210:211]
	v_pk_mul_f32 v[212:213], v[94:95], v[170:171] op_sel_hi:[1,0]
	v_pk_mul_f32 v[214:215], v[96:97], v[170:171] op_sel_hi:[1,0]
	s_waitcnt lgkmcnt(0)
	v_pk_mul_f32 v[224:225], v[146:147], v[216:217]
	v_pk_mul_f32 v[218:219], v[92:93], v[170:171] op_sel_hi:[1,0]
	s_waitcnt lgkmcnt(0)
	v_pk_fma_f32 v[224:225], v[154:155], v[210:211], v[224:225] neg_lo:[0,0,1] neg_hi:[0,0,1]
	v_pk_mul_f32 v[154:155], v[154:155], v[216:217]
	v_pk_mul_f32 v[204:205], v[120:121], v[170:171] op_sel_hi:[1,0]
	v_pk_fma_f32 v[154:155], v[146:147], v[210:211], v[154:155]
	v_lshlrev_b32_e32 v146, 3, v229
	v_pk_mul_f32 v[206:207], v[118:119], v[170:171] op_sel_hi:[1,0]
	v_pk_mul_f32 v[208:209], v[116:117], v[170:171] op_sel_hi:[1,0]
	v_pk_mul_f32 v[214:215], v[136:137], v[214:215]
	v_pk_mul_f32 v[212:213], v[134:135], v[212:213]
	v_pk_mul_f32 v[218:219], v[132:133], v[218:219]
	v_and_b32_e32 v146, 0xf8, v146
	v_pk_mul_f32 v[206:207], v[142:143], v[206:207]
	v_pk_mul_f32 v[204:205], v[144:145], v[204:205]
	v_pk_mul_f32 v[208:209], v[140:141], v[208:209]
	v_pk_mul_f32 v[220:221], v[150:151], v[212:213]
	v_pk_mul_f32 v[222:223], v[152:153], v[214:215]
	v_pk_mul_f32 v[226:227], v[148:149], v[218:219]
	v_or3_b32 v146, v228, v146, v184
	s_waitcnt lgkmcnt(0)
	v_pk_fma_f32 v[222:223], v[160:161], v[204:205], v[222:223] neg_lo:[0,0,1] neg_hi:[0,0,1]
	v_pk_fma_f32 v[220:221], v[158:159], v[206:207], v[220:221] neg_lo:[0,0,1] neg_hi:[0,0,1]
	v_pk_fma_f32 v[226:227], v[156:157], v[208:209], v[226:227] neg_lo:[0,0,1] neg_hi:[0,0,1]
	v_pk_mul_f32 v[158:159], v[158:159], v[212:213]
	v_pk_mul_f32 v[160:161], v[160:161], v[214:215]
	v_pk_mul_f32 v[156:157], v[156:157], v[218:219]
	v_ashrrev_i32_e32 v147, 31, v146
	v_pk_fma_f32 v[152:153], v[152:153], v[204:205], v[160:161]
	v_pk_fma_f32 v[150:151], v[150:151], v[206:207], v[158:159]
	v_pk_fma_f32 v[156:157], v[148:149], v[208:209], v[156:157]
	v_lshl_add_u64 v[158:159], v[146:147], 1, s[54:55]
	v_cvt_pk_f16_f32 v146, v220, v221
	v_cvt_pk_f16_f32 v147, v222, v223
	v_cvt_pk_f16_f32 v148, v224, v225
	v_cvt_pk_f16_f32 v149, v226, v227
	v_bitop3_b32 v184, v199, s74, 32 bitop3:0xc8
	v_cvt_pk_f16_f32 v150, v150, v151
	v_cvt_pk_f16_f32 v151, v152, v153
	v_cvt_pk_f16_f32 v152, v154, v155
	v_cvt_pk_f16_f32 v153, v156, v157
	global_store_dwordx4 v[158:159], v[146:149], off sc1
	v_lshlrev_b32_e32 v170, 7, v184
	v_mul_f32_e32 v204, v105, v105
	v_lshl_add_u64 v[146:147], v[158:159], 0, s[10:11]
	global_store_dwordx4 v[146:147], v[150:153], off sc1
	v_fmac_f32_e32 v204, v104, v104
	ds_read_b128 v[146:149], v245 offset:1024
	ds_read_b128 v[154:157], v244 offset:1024
	s_nop 0
	ds_read_b128 v[150:153], v245 offset:33792
	s_nop 0
	ds_read_b128 v[158:161], v244 offset:33792
	v_mul_f32_e32 v170, v103, v103
	v_fmac_f32_e32 v170, v102, v102
	v_add_f32_e32 v170, v170, v204
	v_pk_mul_f32 v[204:205], v[100:101], v[100:101]
	v_pk_mul_f32 v[206:207], v[98:99], v[98:99]
	v_mov_b32_e32 v208, v204
	v_mov_b32_e32 v209, v206
	v_mov_b32_e32 v206, v205
	v_pk_add_f32 v[204:205], v[208:209], v[206:207]
	v_pk_mul_f32 v[206:207], v[78:79], v[78:79]
	v_add_f32_e32 v170, v170, v205
	v_add_f32_e32 v170, v204, v170
	v_pk_mul_f32 v[204:205], v[80:81], v[80:81]
	v_mov_b32_e32 v209, v206
	v_mov_b32_e32 v208, v204
	v_mov_b32_e32 v206, v205
	v_pk_add_f32 v[204:205], v[208:209], v[206:207]
	v_pk_mul_f32 v[206:207], v[74:75], v[74:75]
	v_add_f32_e32 v170, v170, v205
	v_add_f32_e32 v170, v204, v170
	v_pk_mul_f32 v[204:205], v[76:77], v[76:77]
	v_mov_b32_e32 v209, v206
	v_mov_b32_e32 v208, v204
	v_mov_b32_e32 v206, v205
	v_pk_add_f32 v[204:205], v[208:209], v[206:207]
	s_mov_b64 vcc, s[4:5]
	v_add_f32_e32 v170, v205, v170
	v_add_f32_e32 v170, v204, v170
	ds_bpermute_b32 v204, v201, v170
	v_lshlrev_b32_e32 v205, 6, v184
	s_waitcnt lgkmcnt(0)
	v_add_f32_e32 v170, v170, v204
	ds_bpermute_b32 v204, v202, v170
	s_cbranch_vccnz .LBB1_17
	v_or_b32_e32 v184, 32, v199
	v_lshlrev_b32_e32 v184, 3, v184
	v_and_b32_e32 v206, 0x1f000, v205
	v_and_b32_e32 v184, 0x178, v184
	v_or3_b32 v184, v206, v184, v203
	s_mov_b64 s[8:9], 0

.LBB1_20:
	s_waitcnt lgkmcnt(0)
	v_add_f32_e32 v170, v170, v204
	v_fmamk_f32 v170, v170, 0x3c800000, v195
	v_rsq_f32_e32 v240, v170
	s_nop 0
	v_mul_f32_e32 v242, v170, v240
	v_fma_f32 v242, -v242, v240, 1.0
	v_mul_f32_e32 v243, 0.5, v240
	v_fmac_f32_e32 v240, v242, v243
	v_mul_f32_e32 v170, v200, v240
	s_lshl_b32 s10, s56, 1
	v_add_u32_e32 v228, 0x80, v199
	v_pk_mul_f32 v[212:213], v[78:79], v[170:171] op_sel_hi:[1,0]
	v_pk_mul_f32 v[214:215], v[80:81], v[170:171] op_sel_hi:[1,0]
	v_pk_mul_f32 v[216:217], v[74:75], v[170:171] op_sel_hi:[1,0]
	v_pk_mul_f32 v[218:219], v[76:77], v[170:171] op_sel_hi:[1,0]
	v_pk_mul_f32 v[204:205], v[104:105], v[170:171] op_sel_hi:[1,0]
	v_pk_mul_f32 v[206:207], v[102:103], v[170:171] op_sel_hi:[1,0]
	v_pk_mul_f32 v[208:209], v[100:101], v[170:171] op_sel_hi:[1,0]
	v_pk_mul_f32 v[210:211], v[98:99], v[170:171] op_sel_hi:[1,0]
	v_pk_mul_f32 v[214:215], v[136:137], v[214:215]
	v_pk_mul_f32 v[212:213], v[134:135], v[212:213]
	v_pk_mul_f32 v[218:219], v[132:133], v[218:219]
	v_pk_mul_f32 v[216:217], v[130:131], v[216:217]
	v_pk_mul_f32 v[206:207], v[142:143], v[206:207]
	v_pk_mul_f32 v[204:205], v[144:145], v[204:205]
	v_pk_mul_f32 v[210:211], v[138:139], v[210:211]
	v_pk_mul_f32 v[208:209], v[140:141], v[208:209]
	s_waitcnt lgkmcnt(0)
	v_pk_mul_f32 v[220:221], v[158:159], v[212:213]
	v_pk_mul_f32 v[222:223], v[160:161], v[214:215]
	v_pk_mul_f32 v[224:225], v[150:151], v[216:217]
	v_pk_mul_f32 v[226:227], v[152:153], v[218:219]
	v_pk_fma_f32 v[222:223], v[156:157], v[204:205], v[222:223] neg_lo:[0,0,1] neg_hi:[0,0,1]
	v_pk_fma_f32 v[220:221], v[154:155], v[206:207], v[220:221] neg_lo:[0,0,1] neg_hi:[0,0,1]
	v_pk_fma_f32 v[226:227], v[148:149], v[208:209], v[226:227] neg_lo:[0,0,1] neg_hi:[0,0,1]
	v_pk_fma_f32 v[224:225], v[146:147], v[210:211], v[224:225] neg_lo:[0,0,1] neg_hi:[0,0,1]
	v_pk_mul_f32 v[154:155], v[154:155], v[212:213]
	v_pk_mul_f32 v[156:157], v[156:157], v[214:215]
	v_pk_mul_f32 v[146:147], v[146:147], v[216:217]
	v_pk_mul_f32 v[148:149], v[148:149], v[218:219]
	v_ashrrev_i32_e32 v185, 31, v184
	v_pk_fma_f32 v[156:157], v[160:161], v[204:205], v[156:157]
	v_pk_fma_f32 v[154:155], v[158:159], v[206:207], v[154:155]
	v_pk_fma_f32 v[158:159], v[152:153], v[208:209], v[148:149]
	v_pk_fma_f32 v[152:153], v[150:151], v[210:211], v[146:147]
	v_lshl_add_u64 v[160:161], v[184:185], 1, s[8:9]
	v_cvt_pk_f16_f32 v146, v220, v221
	v_cvt_pk_f16_f32 v147, v222, v223
	v_cvt_pk_f16_f32 v148, v224, v225
	v_cvt_pk_f16_f32 v149, v226, v227
	v_cvt_pk_f16_f32 v150, v154, v155
	v_cvt_pk_f16_f32 v151, v156, v157
	v_cvt_pk_f16_f32 v152, v152, v153
	v_cvt_pk_f16_f32 v153, v158, v159
	global_store_dwordx4 v[160:161], v[146:149], off sc1
	v_bitop3_b32 v226, v199, s75, 48 bitop3:0xc8
	v_lshlrev_b32_e32 v170, 7, v226
	v_lshl_add_u64 v[146:147], v[160:161], 0, s[10:11]
	global_store_dwordx4 v[146:147], v[150:153], off sc1
	v_mul_f32_e32 v146, v87, v87
	v_mul_f32_e32 v147, v89, v89
	v_fmac_f32_e32 v146, v86, v86
	v_fmac_f32_e32 v147, v88, v88
	v_add_f32_e32 v152, v146, v147
	v_pk_mul_f32 v[146:147], v[84:85], v[84:85]
	v_pk_mul_f32 v[148:149], v[82:83], v[82:83]
	v_mov_b32_e32 v150, v146
	v_mov_b32_e32 v151, v148
	v_mov_b32_e32 v148, v147
	v_pk_add_f32 v[146:147], v[150:151], v[148:149]
	v_add_f32_e32 v147, v152, v147
	v_add_f32_e32 v208, v146, v147
	ds_read_b128 v[146:149], v245 offset:50176
	s_nop 0
	ds_read_b128 v[150:153], v244 offset:50176
	s_nop 0
	ds_read_b128 v[154:157], v245 offset:17408
	s_nop 0
	ds_read_b128 v[158:161], v244 offset:17408
	v_pk_mul_f32 v[184:185], v[72:73], v[72:73]
	v_pk_mul_f32 v[204:205], v[70:71], v[70:71]
	v_mov_b32_e32 v206, v184
	v_mov_b32_e32 v207, v204
	v_mov_b32_e32 v204, v185
	v_pk_add_f32 v[184:185], v[206:207], v[204:205]
	v_pk_mul_f32 v[204:205], v[66:67], v[66:67]
	v_add_f32_e32 v170, v208, v185
	v_add_f32_e32 v170, v184, v170
	v_pk_mul_f32 v[184:185], v[68:69], v[68:69]
	v_mov_b32_e32 v207, v204
	v_mov_b32_e32 v206, v184
	v_mov_b32_e32 v204, v185
	v_pk_add_f32 v[184:185], v[206:207], v[204:205]
	v_or_b32_e32 v227, 48, v199
	v_add_f32_e32 v170, v185, v170
	v_add_f32_e32 v170, v184, v170
	ds_bpermute_b32 v184, v201, v170
	s_waitcnt lgkmcnt(0)
	v_add_f32_e32 v170, v170, v184
	ds_bpermute_b32 v184, v202, v170
	s_waitcnt lgkmcnt(0)
	v_add_f32_e32 v170, v170, v184
	v_fmamk_f32 v170, v170, 0x3c800000, v195
	v_rsq_f32_e32 v240, v170
	s_nop 0
	v_mul_f32_e32 v242, v170, v240
	v_fma_f32 v242, -v242, v240, 1.0
	v_mul_f32_e32 v243, 0.5, v240
	v_fmac_f32_e32 v240, v242, v243
	v_mul_f32_e32 v170, v200, v240
	v_pk_mul_f32 v[214:215], v[66:67], v[170:171] op_sel_hi:[1,0]
	v_pk_mul_f32 v[208:209], v[82:83], v[170:171] op_sel_hi:[1,0]
	v_pk_mul_f32 v[214:215], v[130:131], v[214:215]
	v_pk_mul_f32 v[208:209], v[138:139], v[208:209]
	s_waitcnt lgkmcnt(0)
	v_pk_mul_f32 v[222:223], v[146:147], v[214:215]
	v_pk_mul_f32 v[210:211], v[70:71], v[170:171] op_sel_hi:[1,0]
	s_waitcnt lgkmcnt(0)
	v_pk_fma_f32 v[222:223], v[154:155], v[208:209], v[222:223] neg_lo:[0,0,1] neg_hi:[0,0,1]
	v_pk_mul_f32 v[154:155], v[154:155], v[214:215]
	v_pk_mul_f32 v[212:213], v[72:73], v[170:171] op_sel_hi:[1,0]
	v_pk_mul_f32 v[216:217], v[68:69], v[170:171] op_sel_hi:[1,0]
	v_pk_fma_f32 v[154:155], v[146:147], v[208:209], v[154:155]
	v_lshlrev_b32_e32 v146, 6, v226
	v_lshlrev_b32_e32 v147, 3, v227
	v_pk_mul_f32 v[184:185], v[88:89], v[170:171] op_sel_hi:[1,0]
	v_pk_mul_f32 v[204:205], v[86:87], v[170:171] op_sel_hi:[1,0]
	v_pk_mul_f32 v[206:207], v[84:85], v[170:171] op_sel_hi:[1,0]
	v_pk_mul_f32 v[212:213], v[136:137], v[212:213]
	v_pk_mul_f32 v[210:211], v[134:135], v[210:211]
	v_pk_mul_f32 v[216:217], v[132:133], v[216:217]
	v_and_b32_e32 v146, s79, v146
	v_and_b32_e32 v147, s57, v147
	v_pk_mul_f32 v[204:205], v[142:143], v[204:205]
	v_pk_mul_f32 v[184:185], v[144:145], v[184:185]
	v_pk_mul_f32 v[206:207], v[140:141], v[206:207]
	v_pk_mul_f32 v[218:219], v[150:151], v[210:211]
	v_pk_mul_f32 v[220:221], v[152:153], v[212:213]
	v_pk_mul_f32 v[224:225], v[148:149], v[216:217]
	v_or3_b32 v146, v147, v203, v146
	s_waitcnt lgkmcnt(0)
	v_pk_fma_f32 v[220:221], v[160:161], v[184:185], v[220:221] neg_lo:[0,0,1] neg_hi:[0,0,1]
	v_pk_fma_f32 v[218:219], v[158:159], v[204:205], v[218:219] neg_lo:[0,0,1] neg_hi:[0,0,1]
	v_pk_fma_f32 v[224:225], v[156:157], v[206:207], v[224:225] neg_lo:[0,0,1] neg_hi:[0,0,1]
	v_pk_mul_f32 v[158:159], v[158:159], v[210:211]
	v_pk_mul_f32 v[160:161], v[160:161], v[212:213]
	v_pk_mul_f32 v[156:157], v[156:157], v[216:217]
	v_ashrrev_i32_e32 v147, 31, v146
	v_pk_fma_f32 v[152:153], v[152:153], v[184:185], v[160:161]
	v_pk_fma_f32 v[150:151], v[150:151], v[204:205], v[158:159]
	v_pk_fma_f32 v[156:157], v[148:149], v[206:207], v[156:157]
	v_lshl_add_u64 v[158:159], v[146:147], 1, s[8:9]
	v_cvt_pk_f16_f32 v146, v218, v219
	v_cvt_pk_f16_f32 v147, v220, v221
	v_cvt_pk_f16_f32 v148, v222, v223
	v_cvt_pk_f16_f32 v149, v224, v225
	v_cvt_pk_f16_f32 v150, v150, v151
	v_cvt_pk_f16_f32 v151, v152, v153
	v_cvt_pk_f16_f32 v152, v154, v155
	v_cvt_pk_f16_f32 v153, v156, v157
	global_store_dwordx4 v[158:159], v[146:149], off sc1
	v_pk_mul_f32 v[184:185], v[48:49], v[48:49]
	v_pk_mul_f32 v[204:205], v[46:47], v[46:47]
	v_lshl_add_u64 v[146:147], v[158:159], 0, s[10:11]
	global_store_dwordx4 v[146:147], v[150:153], off sc1
	v_mul_f32_e32 v146, v63, v63
	v_mul_f32_e32 v147, v65, v65
	v_fmac_f32_e32 v146, v62, v62
	v_fmac_f32_e32 v147, v64, v64
	v_add_f32_e32 v153, v146, v147
	v_pk_mul_f32 v[146:147], v[60:61], v[60:61]
	v_pk_mul_f32 v[148:149], v[58:59], v[58:59]
	v_and_b32_e32 v152, 0x7cf, v228
	v_mov_b32_e32 v150, v146
	v_mov_b32_e32 v151, v148
	v_mov_b32_e32 v148, v147
	v_pk_add_f32 v[146:147], v[150:151], v[148:149]
	v_lshlrev_b32_e32 v170, 7, v152
	v_add_f32_e32 v147, v153, v147
	v_add_f32_e32 v203, v146, v147
	ds_read_b128 v[146:149], v245 offset:34816
	s_nop 0
	ds_read_b128 v[150:153], v244 offset:34816
	s_nop 0
	ds_read_b128 v[154:157], v245 offset:2048
	s_nop 0
	ds_read_b128 v[158:161], v244 offset:2048
	v_mov_b32_e32 v206, v184
	v_mov_b32_e32 v207, v204
	v_mov_b32_e32 v204, v185
	v_pk_add_f32 v[184:185], v[206:207], v[204:205]
	v_pk_mul_f32 v[204:205], v[42:43], v[42:43]
	v_add_f32_e32 v170, v203, v185
	v_add_f32_e32 v170, v184, v170
	v_pk_mul_f32 v[184:185], v[44:45], v[44:45]
	v_mov_b32_e32 v207, v204
	v_mov_b32_e32 v206, v184
	v_mov_b32_e32 v204, v185
	v_pk_add_f32 v[184:185], v[206:207], v[204:205]
	s_nop 0
	v_add_f32_e32 v170, v185, v170
	v_add_f32_e32 v170, v184, v170
	ds_bpermute_b32 v184, v201, v170
	v_lshrrev_b32_e32 v185, 8, v228
	v_and_b32_e32 v185, 0x7ff8, v185
	v_add_u32_e32 v185, s78, v185
	v_lshl_or_b32 v203, v185, 17, v187
	s_waitcnt lgkmcnt(0)
	v_add_f32_e32 v170, v170, v184
	ds_bpermute_b32 v184, v202, v170
	v_lshrrev_b32_e32 v185, 6, v228
	v_and_b32_e32 v185, 0x7fe0, v185
	v_add_u32_e32 v185, s37, v185
	v_lshl_or_b32 v185, v185, 17, v188
	s_waitcnt lgkmcnt(0)
	v_add_f32_e32 v170, v170, v184
	v_fmamk_f32 v170, v170, 0x3c800000, v195
	v_rsq_f32_e32 v240, v170
	s_nop 0
	v_mul_f32_e32 v242, v170, v240
	v_fma_f32 v242, -v242, v240, 1.0
	v_mul_f32_e32 v243, 0.5, v240
	v_fmac_f32_e32 v240, v242, v243
	v_mul_f32_e32 v170, v200, v240
	v_pk_mul_f32 v[216:217], v[42:43], v[170:171] op_sel_hi:[1,0]
	v_pk_mul_f32 v[210:211], v[58:59], v[170:171] op_sel_hi:[1,0]
	v_pk_mul_f32 v[216:217], v[130:131], v[216:217]
	v_pk_mul_f32 v[210:211], v[138:139], v[210:211]
	v_pk_mul_f32 v[212:213], v[46:47], v[170:171] op_sel_hi:[1,0]
	v_pk_mul_f32 v[214:215], v[48:49], v[170:171] op_sel_hi:[1,0]
	s_waitcnt lgkmcnt(0)
	v_pk_mul_f32 v[224:225], v[146:147], v[216:217]
	v_pk_mul_f32 v[218:219], v[44:45], v[170:171] op_sel_hi:[1,0]
	s_waitcnt lgkmcnt(0)
	v_pk_fma_f32 v[224:225], v[154:155], v[210:211], v[224:225] neg_lo:[0,0,1] neg_hi:[0,0,1]
	v_pk_mul_f32 v[154:155], v[154:155], v[216:217]
	v_pk_mul_f32 v[204:205], v[64:65], v[170:171] op_sel_hi:[1,0]
	v_pk_fma_f32 v[154:155], v[146:147], v[210:211], v[154:155]
	v_lshlrev_b32_e32 v146, 6, v228
	v_pk_mul_f32 v[206:207], v[62:63], v[170:171] op_sel_hi:[1,0]
	v_pk_mul_f32 v[208:209], v[60:61], v[170:171] op_sel_hi:[1,0]
	v_pk_mul_f32 v[214:215], v[136:137], v[214:215]
	v_pk_mul_f32 v[212:213], v[134:135], v[212:213]
	v_pk_mul_f32 v[218:219], v[132:133], v[218:219]
	v_cndmask_b32_e64 v184, v203, v185, s[6:7]
	v_and_b32_e32 v146, 0x1f000, v146
	v_pk_mul_f32 v[206:207], v[142:143], v[206:207]
	v_pk_mul_f32 v[204:205], v[144:145], v[204:205]
	v_pk_mul_f32 v[208:209], v[140:141], v[208:209]
	v_pk_mul_f32 v[220:221], v[150:151], v[212:213]
	v_pk_mul_f32 v[222:223], v[152:153], v[214:215]
	v_pk_mul_f32 v[226:227], v[148:149], v[218:219]
	v_or3_b32 v146, v146, v189, v184
	s_waitcnt lgkmcnt(0)
	v_pk_fma_f32 v[222:223], v[160:161], v[204:205], v[222:223] neg_lo:[0,0,1] neg_hi:[0,0,1]
	v_pk_fma_f32 v[220:221], v[158:159], v[206:207], v[220:221] neg_lo:[0,0,1] neg_hi:[0,0,1]
	v_pk_fma_f32 v[226:227], v[156:157], v[208:209], v[226:227] neg_lo:[0,0,1] neg_hi:[0,0,1]
	v_pk_mul_f32 v[158:159], v[158:159], v[212:213]
	v_pk_mul_f32 v[160:161], v[160:161], v[214:215]
	v_pk_mul_f32 v[156:157], v[156:157], v[218:219]
	v_ashrrev_i32_e32 v147, 31, v146
	v_pk_fma_f32 v[152:153], v[152:153], v[204:205], v[160:161]
	v_pk_fma_f32 v[150:151], v[150:151], v[206:207], v[158:159]
	v_pk_fma_f32 v[156:157], v[148:149], v[208:209], v[156:157]
	v_lshl_add_u64 v[158:159], v[146:147], 1, s[54:55]
	v_cvt_pk_f16_f32 v146, v220, v221
	v_cvt_pk_f16_f32 v147, v222, v223
	v_cvt_pk_f16_f32 v148, v224, v225
	v_cvt_pk_f16_f32 v149, v226, v227
	v_cvt_pk_f16_f32 v150, v150, v151
	v_cvt_pk_f16_f32 v151, v152, v153
	v_cvt_pk_f16_f32 v152, v154, v155
	v_cvt_pk_f16_f32 v153, v156, v157
	global_store_dwordx4 v[158:159], v[146:149], off sc1
	v_add_u32_e32 v228, 0x90, v199
	v_pk_mul_f32 v[204:205], v[32:33], v[32:33]
	v_lshl_add_u64 v[146:147], v[158:159], 0, s[10:11]
	global_store_dwordx4 v[146:147], v[150:153], off sc1
	v_mul_f32_e32 v146, v55, v55
	v_mul_f32_e32 v147, v57, v57
	v_fmac_f32_e32 v146, v54, v54
	v_fmac_f32_e32 v147, v56, v56
	v_add_f32_e32 v153, v146, v147
	v_pk_mul_f32 v[146:147], v[52:53], v[52:53]
	v_pk_mul_f32 v[148:149], v[50:51], v[50:51]
	v_and_b32_e32 v152, 0x7df, v228
	v_mov_b32_e32 v150, v146
	v_mov_b32_e32 v151, v148
	v_mov_b32_e32 v148, v147
	v_pk_add_f32 v[146:147], v[150:151], v[148:149]
	v_lshlrev_b32_e32 v170, 7, v152
	v_add_f32_e32 v147, v153, v147
	v_add_f32_e32 v210, v146, v147
	ds_read_b128 v[146:149], v245 offset:51200
	s_nop 0
	ds_read_b128 v[150:153], v244 offset:51200
	s_nop 0
	ds_read_b128 v[154:157], v245 offset:18432
	s_nop 0
	ds_read_b128 v[158:161], v244 offset:18432
	v_pk_mul_f32 v[206:207], v[30:31], v[30:31]
	v_mov_b32_e32 v208, v204
	v_mov_b32_e32 v209, v206
	v_mov_b32_e32 v206, v205
	v_pk_add_f32 v[204:205], v[208:209], v[206:207]
	v_pk_mul_f32 v[206:207], v[26:27], v[26:27]
	v_add_f32_e32 v170, v210, v205
	v_add_f32_e32 v170, v204, v170
	v_pk_mul_f32 v[204:205], v[28:29], v[28:29]
	v_mov_b32_e32 v209, v206
	v_mov_b32_e32 v208, v204
	v_mov_b32_e32 v206, v205
	v_pk_add_f32 v[204:205], v[208:209], v[206:207]
	s_nop 0
	v_add_f32_e32 v170, v205, v170
	v_add_f32_e32 v170, v204, v170
	ds_bpermute_b32 v204, v201, v170
	s_waitcnt lgkmcnt(0)
	v_add_f32_e32 v170, v170, v204
	ds_bpermute_b32 v204, v202, v170
	s_waitcnt lgkmcnt(0)
	v_add_f32_e32 v170, v170, v204
	v_fmamk_f32 v170, v170, 0x3c800000, v195
	v_rsq_f32_e32 v240, v170
	s_nop 0
	v_mul_f32_e32 v242, v170, v240
	v_fma_f32 v242, -v242, v240, 1.0
	v_mul_f32_e32 v243, 0.5, v240
	v_fmac_f32_e32 v240, v242, v243
	v_mul_f32_e32 v170, v200, v240
	s_mov_b64 s[4:5], -1
	v_pk_mul_f32 v[216:217], v[26:27], v[170:171] op_sel_hi:[1,0]
	v_pk_mul_f32 v[210:211], v[50:51], v[170:171] op_sel_hi:[1,0]
	v_pk_mul_f32 v[216:217], v[130:131], v[216:217]
	v_pk_mul_f32 v[210:211], v[138:139], v[210:211]
	v_pk_mul_f32 v[214:215], v[32:33], v[170:171] op_sel_hi:[1,0]
	s_waitcnt lgkmcnt(0)
	v_pk_mul_f32 v[224:225], v[146:147], v[216:217]
	v_pk_mul_f32 v[204:205], v[56:57], v[170:171] op_sel_hi:[1,0]
	s_waitcnt lgkmcnt(0)
	v_pk_fma_f32 v[224:225], v[154:155], v[210:211], v[224:225] neg_lo:[0,0,1] neg_hi:[0,0,1]
	v_pk_mul_f32 v[154:155], v[154:155], v[216:217]
	v_pk_mul_f32 v[212:213], v[30:31], v[170:171] op_sel_hi:[1,0]
	v_pk_mul_f32 v[214:215], v[136:137], v[214:215]
	v_pk_mul_f32 v[218:219], v[28:29], v[170:171] op_sel_hi:[1,0]
	v_pk_fma_f32 v[154:155], v[146:147], v[210:211], v[154:155]
	v_lshlrev_b32_e32 v146, 6, v228
	v_lshlrev_b32_e32 v147, 3, v228
	v_pk_mul_f32 v[206:207], v[54:55], v[170:171] op_sel_hi:[1,0]
	v_pk_mul_f32 v[204:205], v[144:145], v[204:205]
	v_pk_mul_f32 v[208:209], v[52:53], v[170:171] op_sel_hi:[1,0]
	v_pk_mul_f32 v[212:213], v[134:135], v[212:213]
	v_pk_mul_f32 v[218:219], v[132:133], v[218:219]
	v_pk_mul_f32 v[222:223], v[152:153], v[214:215]
	v_and_b32_e32 v146, 0x1f000, v146
	v_and_b32_e32 v147, 0xf8, v147
	v_pk_mul_f32 v[206:207], v[142:143], v[206:207]
	v_pk_mul_f32 v[208:209], v[140:141], v[208:209]
	v_pk_mul_f32 v[220:221], v[150:151], v[212:213]
	s_waitcnt lgkmcnt(0)
	v_pk_fma_f32 v[222:223], v[160:161], v[204:205], v[222:223] neg_lo:[0,0,1] neg_hi:[0,0,1]
	v_pk_mul_f32 v[226:227], v[148:149], v[218:219]
	v_pk_mul_f32 v[160:161], v[160:161], v[214:215]
	v_or3_b32 v146, v146, v147, v184
	v_pk_fma_f32 v[220:221], v[158:159], v[206:207], v[220:221] neg_lo:[0,0,1] neg_hi:[0,0,1]
	v_pk_fma_f32 v[226:227], v[156:157], v[208:209], v[226:227] neg_lo:[0,0,1] neg_hi:[0,0,1]
	v_pk_mul_f32 v[158:159], v[158:159], v[212:213]
	v_pk_fma_f32 v[152:153], v[152:153], v[204:205], v[160:161]
	v_pk_mul_f32 v[156:157], v[156:157], v[218:219]
	v_ashrrev_i32_e32 v147, 31, v146
	v_add_u32_e32 v204, 0xa0, v199
	v_pk_fma_f32 v[150:151], v[150:151], v[206:207], v[158:159]
	v_pk_fma_f32 v[156:157], v[148:149], v[208:209], v[156:157]
	v_lshl_add_u64 v[158:159], v[146:147], 1, s[54:55]
	v_cvt_pk_f16_f32 v146, v220, v221
	v_cvt_pk_f16_f32 v147, v222, v223
	v_cvt_pk_f16_f32 v148, v224, v225
	v_cvt_pk_f16_f32 v149, v226, v227
	v_and_b32_e32 v184, 0x7ef, v204
	v_cvt_pk_f16_f32 v150, v150, v151
	v_cvt_pk_f16_f32 v151, v152, v153
	v_cvt_pk_f16_f32 v152, v154, v155
	v_cvt_pk_f16_f32 v153, v156, v157
	global_store_dwordx4 v[158:159], v[146:149], off sc1
	v_lshlrev_b32_e32 v170, 7, v184
	v_mul_f32_e32 v205, v41, v41
	v_lshl_add_u64 v[146:147], v[158:159], 0, s[10:11]
	global_store_dwordx4 v[146:147], v[150:153], off sc1
	v_pk_mul_f32 v[206:207], v[36:37], v[36:37]
	ds_read_b128 v[146:149], v245 offset:3072
	ds_read_b128 v[154:157], v244 offset:3072
	s_nop 0
	ds_read_b128 v[150:153], v245 offset:35840
	s_nop 0
	ds_read_b128 v[158:161], v244 offset:35840
	v_mul_f32_e32 v170, v39, v39
	v_pk_mul_f32 v[208:209], v[34:35], v[34:35]
	v_fmac_f32_e32 v170, v38, v38
	v_fmac_f32_e32 v205, v40, v40
	v_mov_b32_e32 v210, v206
	v_mov_b32_e32 v211, v208
	v_mov_b32_e32 v208, v207
	v_add_f32_e32 v170, v170, v205
	v_pk_add_f32 v[206:207], v[210:211], v[208:209]
	v_pk_mul_f32 v[208:209], v[14:15], v[14:15]
	v_add_f32_e32 v170, v170, v207
	v_add_f32_e32 v170, v206, v170
	v_pk_mul_f32 v[206:207], v[16:17], v[16:17]
	v_mov_b32_e32 v211, v208
	v_mov_b32_e32 v210, v206
	v_mov_b32_e32 v208, v207
	v_pk_add_f32 v[206:207], v[210:211], v[208:209]
	v_pk_mul_f32 v[208:209], v[10:11], v[10:11]
	v_add_f32_e32 v170, v170, v207
	v_add_f32_e32 v170, v206, v170
	v_pk_mul_f32 v[206:207], v[12:13], v[12:13]
	v_mov_b32_e32 v211, v208
	v_mov_b32_e32 v210, v206
	v_mov_b32_e32 v208, v207
	v_pk_add_f32 v[206:207], v[210:211], v[208:209]
	s_andn2_b64 vcc, exec, s[52:53]
	v_add_f32_e32 v170, v207, v170
	v_add_f32_e32 v170, v206, v170
	ds_bpermute_b32 v205, v201, v170
	v_lshlrev_b32_e32 v206, 6, v184
	s_waitcnt lgkmcnt(0)
	v_add_f32_e32 v170, v170, v205
	ds_bpermute_b32 v205, v202, v170
	s_cbranch_vccnz .LBB1_22
	v_lshlrev_b32_e32 v204, 3, v204
	v_and_b32_e32 v184, 0x1f000, v206
	v_and_b32_e32 v204, 0x178, v204
	v_or3_b32 v184, v184, v204, v203
	s_mov_b64 s[4:5], 0

.LBB1_25:
	s_waitcnt lgkmcnt(0)
	v_add_f32_e32 v170, v170, v205
	v_fmamk_f32 v170, v170, 0x3c800000, v195
	v_rsq_f32_e32 v240, v170
	s_nop 0
	v_mul_f32_e32 v242, v170, v240
	v_fma_f32 v242, -v242, v240, 1.0
	v_mul_f32_e32 v243, 0.5, v240
	v_fmac_f32_e32 v240, v242, v243
	v_mul_f32_e32 v170, v200, v240
	s_lshl_b32 s10, s8, 1
	v_pk_mul_f32 v[212:213], v[14:15], v[170:171] op_sel_hi:[1,0]
	v_pk_mul_f32 v[214:215], v[16:17], v[170:171] op_sel_hi:[1,0]
	v_pk_mul_f32 v[216:217], v[10:11], v[170:171] op_sel_hi:[1,0]
	v_pk_mul_f32 v[218:219], v[12:13], v[170:171] op_sel_hi:[1,0]
	v_pk_mul_f32 v[204:205], v[40:41], v[170:171] op_sel_hi:[1,0]
	v_pk_mul_f32 v[206:207], v[38:39], v[170:171] op_sel_hi:[1,0]
	v_pk_mul_f32 v[208:209], v[36:37], v[170:171] op_sel_hi:[1,0]
	v_pk_mul_f32 v[210:211], v[34:35], v[170:171] op_sel_hi:[1,0]
	v_pk_mul_f32 v[214:215], v[136:137], v[214:215]
	v_pk_mul_f32 v[212:213], v[134:135], v[212:213]
	v_pk_mul_f32 v[218:219], v[132:133], v[218:219]
	v_pk_mul_f32 v[216:217], v[130:131], v[216:217]
	v_pk_mul_f32 v[206:207], v[142:143], v[206:207]
	v_pk_mul_f32 v[204:205], v[144:145], v[204:205]
	v_pk_mul_f32 v[210:211], v[138:139], v[210:211]
	v_pk_mul_f32 v[208:209], v[140:141], v[208:209]
	s_waitcnt lgkmcnt(0)
	v_pk_mul_f32 v[220:221], v[158:159], v[212:213]
	v_pk_mul_f32 v[222:223], v[160:161], v[214:215]
	v_pk_mul_f32 v[224:225], v[150:151], v[216:217]
	v_pk_mul_f32 v[226:227], v[152:153], v[218:219]
	v_pk_fma_f32 v[222:223], v[156:157], v[204:205], v[222:223] neg_lo:[0,0,1] neg_hi:[0,0,1]
	v_pk_fma_f32 v[220:221], v[154:155], v[206:207], v[220:221] neg_lo:[0,0,1] neg_hi:[0,0,1]
	v_pk_fma_f32 v[226:227], v[148:149], v[208:209], v[226:227] neg_lo:[0,0,1] neg_hi:[0,0,1]
	v_pk_fma_f32 v[224:225], v[146:147], v[210:211], v[224:225] neg_lo:[0,0,1] neg_hi:[0,0,1]
	v_pk_mul_f32 v[154:155], v[154:155], v[212:213]
	v_pk_mul_f32 v[156:157], v[156:157], v[214:215]
	v_pk_mul_f32 v[146:147], v[146:147], v[216:217]
	v_pk_mul_f32 v[148:149], v[148:149], v[218:219]
	v_ashrrev_i32_e32 v185, 31, v184
	v_pk_fma_f32 v[156:157], v[160:161], v[204:205], v[156:157]
	v_pk_fma_f32 v[154:155], v[158:159], v[206:207], v[154:155]
	v_pk_fma_f32 v[158:159], v[152:153], v[208:209], v[148:149]
	v_pk_fma_f32 v[152:153], v[150:151], v[210:211], v[146:147]
	v_lshl_add_u64 v[160:161], v[184:185], 1, s[6:7]
	v_cvt_pk_f16_f32 v146, v220, v221
	v_cvt_pk_f16_f32 v147, v222, v223
	v_cvt_pk_f16_f32 v148, v224, v225
	v_cvt_pk_f16_f32 v149, v226, v227
	v_cvt_pk_f16_f32 v150, v154, v155
	v_cvt_pk_f16_f32 v151, v156, v157
	v_cvt_pk_f16_f32 v152, v152, v153
	v_cvt_pk_f16_f32 v153, v158, v159
	global_store_dwordx4 v[160:161], v[146:149], off sc1
	v_add_u32_e32 v208, 0xb0, v199
	v_and_b32_e32 v209, 0x7ff, v208
	v_lshl_add_u64 v[146:147], v[160:161], 0, s[10:11]
	global_store_dwordx4 v[146:147], v[150:153], off sc1
	v_mul_f32_e32 v146, v23, v23
	v_mul_f32_e32 v147, v25, v25
	v_fmac_f32_e32 v146, v22, v22
	v_fmac_f32_e32 v147, v24, v24
	v_add_f32_e32 v152, v146, v147
	v_pk_mul_f32 v[146:147], v[20:21], v[20:21]
	v_pk_mul_f32 v[148:149], v[18:19], v[18:19]
	v_mov_b32_e32 v150, v146
	v_mov_b32_e32 v151, v148
	v_mov_b32_e32 v148, v147
	v_pk_add_f32 v[146:147], v[150:151], v[148:149]
	v_lshlrev_b32_e32 v170, 7, v209
	v_add_f32_e32 v147, v152, v147
	v_add_f32_e32 v210, v146, v147
	ds_read_b128 v[146:149], v245 offset:52224
	s_nop 0
	ds_read_b128 v[150:153], v244 offset:52224
	s_nop 0
	ds_read_b128 v[154:157], v245 offset:19456
	s_nop 0
	ds_read_b128 v[158:161], v244 offset:19456
	v_pk_mul_f32 v[184:185], v[8:9], v[8:9]
	v_pk_mul_f32 v[204:205], v[6:7], v[6:7]
	v_mov_b32_e32 v206, v184
	v_mov_b32_e32 v207, v204
	v_mov_b32_e32 v204, v185
	v_pk_add_f32 v[184:185], v[206:207], v[204:205]
	v_pk_mul_f32 v[204:205], v[2:3], v[2:3]
	v_add_f32_e32 v170, v210, v185
	v_add_f32_e32 v170, v184, v170
	v_pk_mul_f32 v[184:185], v[4:5], v[4:5]
	v_mov_b32_e32 v207, v204
	v_mov_b32_e32 v206, v184
	v_mov_b32_e32 v204, v185
	v_pk_add_f32 v[184:185], v[206:207], v[204:205]
	s_nop 0
	v_add_f32_e32 v170, v185, v170
	v_add_f32_e32 v170, v184, v170
	ds_bpermute_b32 v184, v201, v170
	s_waitcnt lgkmcnt(0)
	v_add_f32_e32 v170, v170, v184
	ds_bpermute_b32 v184, v202, v170
	s_waitcnt lgkmcnt(0)
	v_add_f32_e32 v170, v170, v184
	v_fmamk_f32 v170, v170, 0x3c800000, v195
	v_rsq_f32_e32 v240, v170
	s_nop 0
	v_mul_f32_e32 v242, v170, v240
	v_fma_f32 v242, -v242, v240, 1.0
	v_mul_f32_e32 v243, 0.5, v240
	v_fmac_f32_e32 v240, v242, v243
	v_mul_f32_e32 v170, v200, v240
	v_pk_mul_f32 v[184:185], v[24:25], v[170:171] op_sel_hi:[1,0]
	v_pk_mul_f32 v[200:201], v[22:23], v[170:171] op_sel_hi:[1,0]
	v_pk_mul_f32 v[144:145], v[144:145], v[184:185]
	v_pk_mul_f32 v[184:185], v[20:21], v[170:171] op_sel_hi:[1,0]
	v_pk_mul_f32 v[142:143], v[142:143], v[200:201]
	v_pk_mul_f32 v[140:141], v[140:141], v[184:185]
	v_pk_mul_f32 v[184:185], v[6:7], v[170:171] op_sel_hi:[1,0]
	v_pk_mul_f32 v[200:201], v[18:19], v[170:171] op_sel_hi:[1,0]
	v_pk_mul_f32 v[134:135], v[134:135], v[184:185]
	v_pk_mul_f32 v[184:185], v[2:3], v[170:171] op_sel_hi:[1,0]
	v_pk_mul_f32 v[138:139], v[138:139], v[200:201]
	v_pk_mul_f32 v[130:131], v[130:131], v[184:185]
	v_pk_mul_f32 v[200:201], v[8:9], v[170:171] op_sel_hi:[1,0]
	s_waitcnt lgkmcnt(0)
	v_pk_mul_f32 v[204:205], v[146:147], v[130:131]
	s_waitcnt lgkmcnt(0)
	v_pk_mul_f32 v[130:131], v[154:155], v[130:131]
	v_pk_mul_f32 v[136:137], v[136:137], v[200:201]
	v_pk_mul_f32 v[200:201], v[4:5], v[170:171] op_sel_hi:[1,0]
	v_pk_fma_f32 v[204:205], v[154:155], v[138:139], v[204:205] neg_lo:[0,0,1] neg_hi:[0,0,1]
	v_pk_fma_f32 v[138:139], v[146:147], v[138:139], v[130:131]
	v_lshlrev_b32_e32 v130, 6, v209
	v_lshlrev_b32_e32 v131, 3, v208
	v_pk_mul_f32 v[132:133], v[132:133], v[200:201]
	v_and_b32_e32 v130, s37, v130
	v_and_b32_e32 v131, s9, v131
	v_pk_mul_f32 v[184:185], v[150:151], v[134:135]
	v_pk_mul_f32 v[200:201], v[152:153], v[136:137]
	v_pk_mul_f32 v[206:207], v[148:149], v[132:133]
	v_or3_b32 v130, v131, v203, v130
	s_waitcnt lgkmcnt(0)
	v_pk_fma_f32 v[200:201], v[160:161], v[144:145], v[200:201] neg_lo:[0,0,1] neg_hi:[0,0,1]
	v_pk_fma_f32 v[184:185], v[158:159], v[142:143], v[184:185] neg_lo:[0,0,1] neg_hi:[0,0,1]
	v_pk_fma_f32 v[206:207], v[156:157], v[140:141], v[206:207] neg_lo:[0,0,1] neg_hi:[0,0,1]
	v_pk_mul_f32 v[134:135], v[158:159], v[134:135]
	v_pk_mul_f32 v[136:137], v[160:161], v[136:137]
	v_pk_mul_f32 v[132:133], v[156:157], v[132:133]
	v_ashrrev_i32_e32 v131, 31, v130
	v_pk_fma_f32 v[136:137], v[152:153], v[144:145], v[136:137]
	v_pk_fma_f32 v[134:135], v[150:151], v[142:143], v[134:135]
	v_pk_fma_f32 v[140:141], v[148:149], v[140:141], v[132:133]
	v_lshl_add_u64 v[142:143], v[130:131], 1, s[6:7]
	v_cvt_pk_f16_f32 v130, v184, v185
	v_cvt_pk_f16_f32 v131, v200, v201
	v_cvt_pk_f16_f32 v132, v204, v205
	v_cvt_pk_f16_f32 v133, v206, v207
	v_cvt_pk_f16_f32 v134, v134, v135
	v_cvt_pk_f16_f32 v135, v136, v137
	v_cvt_pk_f16_f32 v136, v138, v139
	v_cvt_pk_f16_f32 v137, v140, v141
	global_store_dwordx4 v[142:143], v[130:133], off sc1
	s_nop 1
	v_lshl_add_u64 v[130:131], v[142:143], 0, s[10:11]
	global_store_dwordx4 v[130:131], v[134:137], off sc1
	s_branch .LBB1_14
